# P4 weight converter: non-temporal hint on the write-once converted-weight stores (fp8 and bf16 paths)
# speedup vs baseline: 1.0078x; 1.0018x over previous
; __device__ __forceinline__ void convert_item(Frame& F, int i0, LAS unsigned char* cvbuf) {
;     { const CvItem c = cv_decode(F, i0);
;         float x[128];
; #pragma unroll
;         for (int i = 0; i < 128; ++i) x[i] = c.src[(size_t)i * c.N];
.LBB0_1092:
	s_lshl_b64 s[16:17], s[16:17], 2
	global_load_dword v16, v[12:13], off
	v_lshl_add_u64 v[12:13], v[12:13], 0, s[16:17]
	v_lshl_add_u64 v[18:19], v[12:13], 0, s[16:17]
	v_lshl_add_u64 v[20:21], v[18:19], 0, s[16:17]
	v_lshl_add_u64 v[22:23], v[20:21], 0, s[16:17]
	v_lshl_add_u64 v[24:25], v[22:23], 0, s[16:17]
	v_lshl_add_u64 v[26:27], v[24:25], 0, s[16:17]
	v_lshl_add_u64 v[28:29], v[26:27], 0, s[16:17]
	v_lshl_add_u64 v[30:31], v[28:29], 0, s[16:17]
	global_load_dword v13, v[12:13], off
	s_nop 0
	global_load_dword v17, v[18:19], off
	s_nop 0
	global_load_dword v18, v[20:21], off
	global_load_dword v19, v[22:23], off
	s_nop 0
	global_load_dword v20, v[24:25], off
	global_load_dword v21, v[26:27], off
	s_nop 0
	global_load_dword v24, v[28:29], off
	global_load_dword v12, v[30:31], off
	v_lshl_add_u64 v[22:23], v[30:31], 0, s[16:17]
	v_lshl_add_u64 v[26:27], v[22:23], 0, s[16:17]
	global_load_dword v22, v[22:23], off
	s_nop 0
	global_load_dword v23, v[26:27], off
	v_lshl_add_u64 v[26:27], v[26:27], 0, s[16:17]
	v_lshl_add_u64 v[28:29], v[26:27], 0, s[16:17]
	v_lshl_add_u64 v[30:31], v[28:29], 0, s[16:17]
	global_load_dword v25, v[26:27], off
	s_andn2_b64 vcc, exec, s[14:15]
	global_load_dword v26, v[28:29], off
	s_mov_b64 s[14:15], -1
	global_load_dword v28, v[30:31], off
	v_lshl_add_u64 v[30:31], v[30:31], 0, s[16:17]
	global_load_dword v29, v[30:31], off
	v_lshl_add_u64 v[30:31], v[30:31], 0, s[16:17]
	global_load_dword v32, v[30:31], off
	v_lshl_add_u64 v[30:31], v[30:31], 0, s[16:17]
	v_lshl_add_u64 v[34:35], v[30:31], 0, s[16:17]
	global_load_dword v27, v[30:31], off
	s_nop 0
	global_load_dword v30, v[34:35], off
	v_lshl_add_u64 v[34:35], v[34:35], 0, s[16:17]
	global_load_dword v31, v[34:35], off
	v_lshl_add_u64 v[34:35], v[34:35], 0, s[16:17]
	v_lshl_add_u64 v[36:37], v[34:35], 0, s[16:17]
	v_lshl_add_u64 v[38:39], v[36:37], 0, s[16:17]
	global_load_dword v33, v[34:35], off
	s_nop 0
	global_load_dword v34, v[36:37], off
	s_nop 0
	global_load_dword v36, v[38:39], off
	v_lshl_add_u64 v[38:39], v[38:39], 0, s[16:17]
	global_load_dword v37, v[38:39], off
	v_lshl_add_u64 v[38:39], v[38:39], 0, s[16:17]
	global_load_dword v40, v[38:39], off
	v_lshl_add_u64 v[38:39], v[38:39], 0, s[16:17]
	v_lshl_add_u64 v[42:43], v[38:39], 0, s[16:17]
	global_load_dword v35, v[38:39], off
	s_nop 0
	global_load_dword v38, v[42:43], off
	v_lshl_add_u64 v[42:43], v[42:43], 0, s[16:17]
	global_load_dword v39, v[42:43], off
	v_lshl_add_u64 v[42:43], v[42:43], 0, s[16:17]
	v_lshl_add_u64 v[44:45], v[42:43], 0, s[16:17]
	v_lshl_add_u64 v[46:47], v[44:45], 0, s[16:17]
	global_load_dword v41, v[42:43], off
	s_nop 0
	global_load_dword v42, v[44:45], off
	s_nop 0
	global_load_dword v44, v[46:47], off
	v_lshl_add_u64 v[46:47], v[46:47], 0, s[16:17]
	global_load_dword v45, v[46:47], off
	v_lshl_add_u64 v[46:47], v[46:47], 0, s[16:17]
	global_load_dword v48, v[46:47], off
	v_lshl_add_u64 v[46:47], v[46:47], 0, s[16:17]
	v_lshl_add_u64 v[50:51], v[46:47], 0, s[16:17]
	global_load_dword v43, v[46:47], off
	s_nop 0
	global_load_dword v46, v[50:51], off
	v_lshl_add_u64 v[50:51], v[50:51], 0, s[16:17]
	global_load_dword v47, v[50:51], off
	v_lshl_add_u64 v[50:51], v[50:51], 0, s[16:17]
	v_lshl_add_u64 v[52:53], v[50:51], 0, s[16:17]
	v_lshl_add_u64 v[54:55], v[52:53], 0, s[16:17]
	global_load_dword v49, v[50:51], off
	s_nop 0
	global_load_dword v50, v[52:53], off
	s_nop 0
	global_load_dword v52, v[54:55], off
	v_lshl_add_u64 v[54:55], v[54:55], 0, s[16:17]
	global_load_dword v53, v[54:55], off
	v_lshl_add_u64 v[54:55], v[54:55], 0, s[16:17]
	global_load_dword v56, v[54:55], off
	v_lshl_add_u64 v[54:55], v[54:55], 0, s[16:17]
	v_lshl_add_u64 v[58:59], v[54:55], 0, s[16:17]
	global_load_dword v51, v[54:55], off
	s_nop 0
	global_load_dword v54, v[58:59], off
	v_lshl_add_u64 v[58:59], v[58:59], 0, s[16:17]
	global_load_dword v55, v[58:59], off
	v_lshl_add_u64 v[58:59], v[58:59], 0, s[16:17]
	v_lshl_add_u64 v[60:61], v[58:59], 0, s[16:17]
	v_lshl_add_u64 v[62:63], v[60:61], 0, s[16:17]
	global_load_dword v57, v[58:59], off
	s_nop 0
	global_load_dword v58, v[60:61], off
	s_nop 0
	global_load_dword v60, v[62:63], off
	v_lshl_add_u64 v[62:63], v[62:63], 0, s[16:17]
	global_load_dword v61, v[62:63], off
	v_lshl_add_u64 v[62:63], v[62:63], 0, s[16:17]
	global_load_dword v64, v[62:63], off
	v_lshl_add_u64 v[62:63], v[62:63], 0, s[16:17]
	v_lshl_add_u64 v[66:67], v[62:63], 0, s[16:17]
	global_load_dword v59, v[62:63], off
	s_nop 0
	global_load_dword v62, v[66:67], off
	v_lshl_add_u64 v[66:67], v[66:67], 0, s[16:17]
	global_load_dword v63, v[66:67], off
	v_lshl_add_u64 v[66:67], v[66:67], 0, s[16:17]
	v_lshl_add_u64 v[68:69], v[66:67], 0, s[16:17]
	v_lshl_add_u64 v[70:71], v[68:69], 0, s[16:17]
	global_load_dword v65, v[66:67], off
	s_nop 0
	global_load_dword v66, v[68:69], off
	s_nop 0
	global_load_dword v68, v[70:71], off
	v_lshl_add_u64 v[70:71], v[70:71], 0, s[16:17]
	global_load_dword v69, v[70:71], off
	v_lshl_add_u64 v[70:71], v[70:71], 0, s[16:17]
	global_load_dword v72, v[70:71], off
	v_lshl_add_u64 v[70:71], v[70:71], 0, s[16:17]
	s_waitcnt vmcnt(62)
; __device__ __forceinline__ void convert_item(Frame& F, int i0, LAS unsigned char* cvbuf) {
;     { const CvItem c = cv_decode(F, i0);
;         float x[128];
; #pragma unroll
;         for (int i = 0; i < 128; ++i) x[i] = c.src[(size_t)i * c.N];
	v_lshl_add_u64 v[74:75], v[70:71], 0, s[16:17]
	global_load_dword v67, v[70:71], off
	s_nop 0
	global_load_dword v70, v[74:75], off
	v_lshl_add_u64 v[74:75], v[74:75], 0, s[16:17]
	global_load_dword v71, v[74:75], off
	v_lshl_add_u64 v[74:75], v[74:75], 0, s[16:17]
	v_lshl_add_u64 v[76:77], v[74:75], 0, s[16:17]
	v_lshl_add_u64 v[78:79], v[76:77], 0, s[16:17]
	global_load_dword v73, v[74:75], off
	s_nop 0
	global_load_dword v74, v[76:77], off
	s_nop 0
	global_load_dword v76, v[78:79], off
	v_lshl_add_u64 v[78:79], v[78:79], 0, s[16:17]
	global_load_dword v77, v[78:79], off
	v_lshl_add_u64 v[78:79], v[78:79], 0, s[16:17]
	global_load_dword v80, v[78:79], off
	v_lshl_add_u64 v[78:79], v[78:79], 0, s[16:17]
	v_lshl_add_u64 v[82:83], v[78:79], 0, s[16:17]
	global_load_dword v75, v[78:79], off
	s_nop 0
	global_load_dword v78, v[82:83], off
	v_lshl_add_u64 v[82:83], v[82:83], 0, s[16:17]
	global_load_dword v79, v[82:83], off
	v_lshl_add_u64 v[82:83], v[82:83], 0, s[16:17]
	v_lshl_add_u64 v[84:85], v[82:83], 0, s[16:17]
	v_lshl_add_u64 v[86:87], v[84:85], 0, s[16:17]
	global_load_dword v81, v[82:83], off
	s_nop 0
	global_load_dword v82, v[84:85], off
	s_nop 0
	global_load_dword v84, v[86:87], off
	v_lshl_add_u64 v[86:87], v[86:87], 0, s[16:17]
	global_load_dword v85, v[86:87], off
	v_lshl_add_u64 v[86:87], v[86:87], 0, s[16:17]
	global_load_dword v88, v[86:87], off
	v_lshl_add_u64 v[86:87], v[86:87], 0, s[16:17]
	v_lshl_add_u64 v[90:91], v[86:87], 0, s[16:17]
	global_load_dword v83, v[86:87], off
	s_nop 0
	global_load_dword v86, v[90:91], off
	v_lshl_add_u64 v[90:91], v[90:91], 0, s[16:17]
	global_load_dword v87, v[90:91], off
	v_lshl_add_u64 v[90:91], v[90:91], 0, s[16:17]
	v_lshl_add_u64 v[92:93], v[90:91], 0, s[16:17]
	v_lshl_add_u64 v[94:95], v[92:93], 0, s[16:17]
	global_load_dword v89, v[90:91], off
	s_nop 0
	global_load_dword v90, v[92:93], off
	s_nop 0
	global_load_dword v92, v[94:95], off
	v_lshl_add_u64 v[94:95], v[94:95], 0, s[16:17]
	global_load_dword v93, v[94:95], off
	v_lshl_add_u64 v[94:95], v[94:95], 0, s[16:17]
	global_load_dword v96, v[94:95], off
	v_lshl_add_u64 v[94:95], v[94:95], 0, s[16:17]
	v_lshl_add_u64 v[98:99], v[94:95], 0, s[16:17]
	global_load_dword v91, v[94:95], off
	s_nop 0
	global_load_dword v94, v[98:99], off
	v_lshl_add_u64 v[98:99], v[98:99], 0, s[16:17]
	global_load_dword v95, v[98:99], off
	v_lshl_add_u64 v[98:99], v[98:99], 0, s[16:17]
	v_lshl_add_u64 v[100:101], v[98:99], 0, s[16:17]
	v_lshl_add_u64 v[102:103], v[100:101], 0, s[16:17]
	global_load_dword v97, v[98:99], off
	s_nop 0
	global_load_dword v98, v[100:101], off
	s_nop 0
	global_load_dword v100, v[102:103], off
	v_lshl_add_u64 v[102:103], v[102:103], 0, s[16:17]
	global_load_dword v101, v[102:103], off
	v_lshl_add_u64 v[102:103], v[102:103], 0, s[16:17]
	global_load_dword v104, v[102:103], off
	v_lshl_add_u64 v[102:103], v[102:103], 0, s[16:17]
	v_lshl_add_u64 v[106:107], v[102:103], 0, s[16:17]
	global_load_dword v99, v[102:103], off
	s_nop 0
	global_load_dword v102, v[106:107], off
	v_lshl_add_u64 v[106:107], v[106:107], 0, s[16:17]
	global_load_dword v103, v[106:107], off
	v_lshl_add_u64 v[106:107], v[106:107], 0, s[16:17]
	v_lshl_add_u64 v[108:109], v[106:107], 0, s[16:17]
	v_lshl_add_u64 v[110:111], v[108:109], 0, s[16:17]
	global_load_dword v105, v[106:107], off
	s_nop 0
	global_load_dword v106, v[108:109], off
	s_nop 0
	global_load_dword v108, v[110:111], off
	v_lshl_add_u64 v[110:111], v[110:111], 0, s[16:17]
	global_load_dword v109, v[110:111], off
	v_lshl_add_u64 v[110:111], v[110:111], 0, s[16:17]
	global_load_dword v112, v[110:111], off
	v_lshl_add_u64 v[110:111], v[110:111], 0, s[16:17]
	v_lshl_add_u64 v[114:115], v[110:111], 0, s[16:17]
	global_load_dword v107, v[110:111], off
	s_nop 0
	global_load_dword v110, v[114:115], off
	v_lshl_add_u64 v[114:115], v[114:115], 0, s[16:17]
	global_load_dword v111, v[114:115], off
	v_lshl_add_u64 v[114:115], v[114:115], 0, s[16:17]
	v_lshl_add_u64 v[116:117], v[114:115], 0, s[16:17]
	v_lshl_add_u64 v[118:119], v[116:117], 0, s[16:17]
	global_load_dword v113, v[114:115], off
	s_nop 0
	global_load_dword v114, v[116:117], off
	s_nop 0
	global_load_dword v116, v[118:119], off
	v_lshl_add_u64 v[118:119], v[118:119], 0, s[16:17]
	global_load_dword v117, v[118:119], off
	v_lshl_add_u64 v[118:119], v[118:119], 0, s[16:17]
	global_load_dword v120, v[118:119], off
	v_lshl_add_u64 v[118:119], v[118:119], 0, s[16:17]
	v_lshl_add_u64 v[122:123], v[118:119], 0, s[16:17]
	global_load_dword v115, v[118:119], off
	s_nop 0
	global_load_dword v118, v[122:123], off
	v_lshl_add_u64 v[122:123], v[122:123], 0, s[16:17]
	global_load_dword v119, v[122:123], off
	v_lshl_add_u64 v[122:123], v[122:123], 0, s[16:17]
	v_lshl_add_u64 v[124:125], v[122:123], 0, s[16:17]
	v_lshl_add_u64 v[126:127], v[124:125], 0, s[16:17]
	global_load_dword v121, v[122:123], off
	s_nop 0
	global_load_dword v122, v[124:125], off
	s_nop 0
	global_load_dword v124, v[126:127], off
	v_lshl_add_u64 v[126:127], v[126:127], 0, s[16:17]
	global_load_dword v125, v[126:127], off
	v_lshl_add_u64 v[126:127], v[126:127], 0, s[16:17]
	global_load_dword v128, v[126:127], off
	v_lshl_add_u64 v[126:127], v[126:127], 0, s[16:17]
	v_lshl_add_u64 v[130:131], v[126:127], 0, s[16:17]
	global_load_dword v123, v[126:127], off
	s_nop 0
	global_load_dword v126, v[130:131], off
	v_lshl_add_u64 v[130:131], v[130:131], 0, s[16:17]
	global_load_dword v127, v[130:131], off
	v_lshl_add_u64 v[130:131], v[130:131], 0, s[16:17]
	v_lshl_add_u64 v[132:133], v[130:131], 0, s[16:17]
	s_waitcnt vmcnt(62)
	v_lshl_add_u64 v[134:135], v[132:133], 0, s[16:17]
	global_load_dword v129, v[130:131], off
	s_nop 0
	global_load_dword v130, v[132:133], off
	s_nop 0
	global_load_dword v132, v[134:135], off
	v_lshl_add_u64 v[134:135], v[134:135], 0, s[16:17]
	global_load_dword v133, v[134:135], off
	v_lshl_add_u64 v[134:135], v[134:135], 0, s[16:17]
	global_load_dword v136, v[134:135], off
	v_lshl_add_u64 v[134:135], v[134:135], 0, s[16:17]
	v_lshl_add_u64 v[138:139], v[134:135], 0, s[16:17]
	global_load_dword v131, v[134:135], off
	s_nop 0
	global_load_dword v134, v[138:139], off
	v_lshl_add_u64 v[138:139], v[138:139], 0, s[16:17]
	global_load_dword v135, v[138:139], off
	v_lshl_add_u64 v[138:139], v[138:139], 0, s[16:17]
	s_waitcnt vmcnt(62)
	v_lshl_add_u64 v[140:141], v[138:139], 0, s[16:17]
	global_load_dword v137, v[138:139], off
	s_nop 0
	global_load_dword v138, v[140:141], off
	v_lshl_add_u64 v[140:141], v[140:141], 0, s[16:17]
	v_lshl_add_u64 v[142:143], v[140:141], 0, s[16:17]
	global_load_dword v139, v[140:141], off
	s_nop 0
	global_load_dword v140, v[142:143], off
	v_lshl_add_u64 v[142:143], v[142:143], 0, s[16:17]
	global_load_dword v141, v[142:143], off
	s_cbranch_vccz .LBB0_1094
; #define LAS __attribute__((address_space(3)))
; __device__ __forceinline__ unsigned pk4f8(float a, float b, float c, float d) { int r = 0; r = __builtin_amdgcn_cvt_pk_fp8_f32(a, b, r, false); r = __builtin_amdgcn_cvt_pk_fp8_f32(c, d, r, true); return (unsigned)r; }
; __device__ __forceinline__ void convert_item(Frame& F, int i0, LAS unsigned char* cvbuf) {
;     ...
;         if (c.f8) {
;             const int lane = F.lane; LAS unsigned char* bw = cvbuf + lane * 144;
; #pragma unroll
;             for (int q = 0; q < 8; ++q) { v4u o; o.x = pk4f8(x[16 * q + 0] * F8_SW, x[16 * q + 1] * F8_SW, x[16 * q + 2] * F8_SW, x[16 * q + 3] * F8_SW); o.y = pk4f8(x[16 * q + 4] * F8_SW, x[16 * q + 5] * F8_SW, x[16 * q + 6] * F8_SW, x[16 * q + 7] * F8_SW);
;                 o.z = pk4f8(x[16 * q + 8] * F8_SW, x[16 * q + 9] * F8_SW, x[16 * q + 10] * F8_SW, x[16 * q + 11] * F8_SW); o.w = pk4f8(x[16 * q + 12] * F8_SW, x[16 * q + 13] * F8_SW, x[16 * q + 14] * F8_SW, x[16 * q + 15] * F8_SW);
;                 *(LAS v4u*)(bw + 16 * q) = o; }
	v_mul_f32_e32 v143, 0x43800000, v16
	v_mul_f32_e32 v144, 0x43800000, v13
	v_mov_b32_e32 v142, v3
	v_cvt_pk_fp8_f32 v142, v143, v144
	v_mul_f32_e32 v144, 0x43800000, v19
	v_mul_f32_e32 v147, 0x43800000, v20
	v_mov_b32_e32 v143, v3
	v_cvt_pk_fp8_f32 v143, v144, v147
	v_mul_f32_e32 v145, 0x43800000, v17
	v_mul_f32_e32 v146, 0x43800000, v18
	v_cvt_pk_fp8_f32 v142, v145, v146 op_sel:[0,0,1]
	v_mul_f32_e32 v144, 0x43800000, v21
	v_mul_f32_e32 v145, 0x43800000, v24
	v_cvt_pk_fp8_f32 v143, v144, v145 op_sel:[0,0,1]
	v_mul_f32_e32 v145, 0x43800000, v12
	v_mul_f32_e32 v146, 0x43800000, v22
	v_mov_b32_e32 v144, v3
	v_cvt_pk_fp8_f32 v144, v145, v146
	v_mul_f32_e32 v146, 0x43800000, v26
	v_mul_f32_e32 v149, 0x43800000, v28
	v_mov_b32_e32 v145, v3
	v_cvt_pk_fp8_f32 v145, v146, v149
	v_mul_f32_e32 v147, 0x43800000, v23
	v_mul_f32_e32 v148, 0x43800000, v25
	v_cvt_pk_fp8_f32 v144, v147, v148 op_sel:[0,0,1]
	v_mul_f32_e32 v146, 0x43800000, v29
	v_mul_f32_e32 v147, 0x43800000, v32
	v_cvt_pk_fp8_f32 v145, v146, v147 op_sel:[0,0,1]
	v_mul_f32_e32 v147, 0x43800000, v27
	v_mul_f32_e32 v148, 0x43800000, v30
	v_mov_b32_e32 v146, v3
	v_cvt_pk_fp8_f32 v146, v147, v148
	v_mul_f32_e32 v148, 0x43800000, v34
	v_mul_f32_e32 v151, 0x43800000, v36
	v_mov_b32_e32 v147, v3
	v_cvt_pk_fp8_f32 v147, v148, v151
	v_mul_f32_e32 v149, 0x43800000, v31
	v_mul_f32_e32 v150, 0x43800000, v33
	v_cvt_pk_fp8_f32 v146, v149, v150 op_sel:[0,0,1]
	v_mul_f32_e32 v148, 0x43800000, v37
	v_mul_f32_e32 v149, 0x43800000, v40
	v_cvt_pk_fp8_f32 v147, v148, v149 op_sel:[0,0,1]
	v_mul_f32_e32 v149, 0x43800000, v35
	v_mul_f32_e32 v150, 0x43800000, v38
	v_mov_b32_e32 v148, v3
	v_cvt_pk_fp8_f32 v148, v149, v150
	v_mul_f32_e32 v150, 0x43800000, v42
	v_mul_f32_e32 v153, 0x43800000, v44
	v_mov_b32_e32 v149, v3
	v_cvt_pk_fp8_f32 v149, v150, v153
	v_mul_f32_e32 v151, 0x43800000, v39
	v_mul_f32_e32 v152, 0x43800000, v41
	v_cvt_pk_fp8_f32 v148, v151, v152 op_sel:[0,0,1]
	v_mul_f32_e32 v150, 0x43800000, v45
	v_mul_f32_e32 v151, 0x43800000, v48
	v_cvt_pk_fp8_f32 v149, v150, v151 op_sel:[0,0,1]
	v_mul_f32_e32 v151, 0x43800000, v43
	v_mul_f32_e32 v152, 0x43800000, v46
	v_mov_b32_e32 v150, v3
	v_cvt_pk_fp8_f32 v150, v151, v152
	v_mul_f32_e32 v152, 0x43800000, v50
	v_mul_f32_e32 v155, 0x43800000, v52
	v_mov_b32_e32 v151, v3
	v_cvt_pk_fp8_f32 v151, v152, v155
	v_mul_f32_e32 v153, 0x43800000, v47
	v_mul_f32_e32 v154, 0x43800000, v49
	v_cvt_pk_fp8_f32 v150, v153, v154 op_sel:[0,0,1]
	v_mul_f32_e32 v152, 0x43800000, v53
	v_mul_f32_e32 v153, 0x43800000, v56
	v_cvt_pk_fp8_f32 v151, v152, v153 op_sel:[0,0,1]
	v_mul_f32_e32 v153, 0x43800000, v51
	v_mul_f32_e32 v154, 0x43800000, v54
	v_mov_b32_e32 v152, v3
	v_cvt_pk_fp8_f32 v152, v153, v154
	v_mul_f32_e32 v154, 0x43800000, v58
	v_mul_f32_e32 v157, 0x43800000, v60
	v_mov_b32_e32 v153, v3
	v_cvt_pk_fp8_f32 v153, v154, v157
	v_mul_f32_e32 v155, 0x43800000, v55
	v_mul_f32_e32 v156, 0x43800000, v57
	v_cvt_pk_fp8_f32 v152, v155, v156 op_sel:[0,0,1]
	v_mul_f32_e32 v154, 0x43800000, v61
	v_mul_f32_e32 v155, 0x43800000, v64
	v_cvt_pk_fp8_f32 v153, v154, v155 op_sel:[0,0,1]
	v_mul_f32_e32 v155, 0x43800000, v59
	v_mul_f32_e32 v156, 0x43800000, v62
	v_mov_b32_e32 v154, v3
	v_cvt_pk_fp8_f32 v154, v155, v156
	v_mul_f32_e32 v156, 0x43800000, v66
	v_mul_f32_e32 v159, 0x43800000, v68
	v_mov_b32_e32 v155, v3
	v_cvt_pk_fp8_f32 v155, v156, v159
	v_mul_f32_e32 v157, 0x43800000, v63
	v_mul_f32_e32 v158, 0x43800000, v65
	v_cvt_pk_fp8_f32 v154, v157, v158 op_sel:[0,0,1]
	v_mul_f32_e32 v156, 0x43800000, v69
	v_mul_f32_e32 v157, 0x43800000, v72
	v_cvt_pk_fp8_f32 v155, v156, v157 op_sel:[0,0,1]
	v_mul_f32_e32 v157, 0x43800000, v67
	v_mul_f32_e32 v158, 0x43800000, v70
	v_mov_b32_e32 v156, v3
	v_cvt_pk_fp8_f32 v156, v157, v158
	v_mul_f32_e32 v158, 0x43800000, v74
	s_waitcnt vmcnt(62)
	v_mul_f32_e32 v161, 0x43800000, v76
	v_mov_b32_e32 v157, v3
	v_cvt_pk_fp8_f32 v157, v158, v161
	v_mul_f32_e32 v159, 0x43800000, v71
	v_mul_f32_e32 v160, 0x43800000, v73
	v_cvt_pk_fp8_f32 v156, v159, v160 op_sel:[0,0,1]
	v_mul_f32_e32 v158, 0x43800000, v77
	v_mul_f32_e32 v159, 0x43800000, v80
	v_cvt_pk_fp8_f32 v157, v158, v159 op_sel:[0,0,1]
	ds_write_b128 v14, v[142:145] offset:8192
	ds_write_b128 v14, v[146:149] offset:8208
	ds_write_b128 v14, v[150:153] offset:8224
	ds_write_b128 v14, v[154:157] offset:8240
	v_mul_f32_e32 v143, 0x43800000, v75
	v_mul_f32_e32 v144, 0x43800000, v78
	v_mov_b32_e32 v142, v3
	v_cvt_pk_fp8_f32 v142, v143, v144
	s_waitcnt vmcnt(59)
	v_mul_f32_e32 v144, 0x43800000, v82
	s_waitcnt vmcnt(58)
	v_mul_f32_e32 v147, 0x43800000, v84
	v_mov_b32_e32 v143, v3
	v_cvt_pk_fp8_f32 v143, v144, v147
	v_mul_f32_e32 v145, 0x43800000, v79
	v_mul_f32_e32 v146, 0x43800000, v81
	v_cvt_pk_fp8_f32 v142, v145, v146 op_sel:[0,0,1]
	s_waitcnt vmcnt(57)
	v_mul_f32_e32 v144, 0x43800000, v85
	s_waitcnt vmcnt(56)
	v_mul_f32_e32 v145, 0x43800000, v88
	v_cvt_pk_fp8_f32 v143, v144, v145 op_sel:[0,0,1]
	s_waitcnt vmcnt(55)
	v_mul_f32_e32 v145, 0x43800000, v83
	s_waitcnt vmcnt(54)
	v_mul_f32_e32 v146, 0x43800000, v86
	v_mov_b32_e32 v144, v3
	v_cvt_pk_fp8_f32 v144, v145, v146
	s_waitcnt vmcnt(51)
	v_mul_f32_e32 v146, 0x43800000, v90
	s_waitcnt vmcnt(50)
	v_mul_f32_e32 v149, 0x43800000, v92
	v_mov_b32_e32 v145, v3
	v_cvt_pk_fp8_f32 v145, v146, v149
	v_mul_f32_e32 v147, 0x43800000, v87
	v_mul_f32_e32 v148, 0x43800000, v89
	v_cvt_pk_fp8_f32 v144, v147, v148 op_sel:[0,0,1]
	s_waitcnt vmcnt(49)
	v_mul_f32_e32 v146, 0x43800000, v93
	s_waitcnt vmcnt(48)
	v_mul_f32_e32 v147, 0x43800000, v96
	v_cvt_pk_fp8_f32 v145, v146, v147 op_sel:[0,0,1]
	s_waitcnt vmcnt(47)
	v_mul_f32_e32 v147, 0x43800000, v91
	s_waitcnt vmcnt(46)
; #define LAS __attribute__((address_space(3)))
; __device__ __forceinline__ unsigned pk4f8(float a, float b, float c, float d) { int r = 0; r = __builtin_amdgcn_cvt_pk_fp8_f32(a, b, r, false); r = __builtin_amdgcn_cvt_pk_fp8_f32(c, d, r, true); return (unsigned)r; }
; __device__ __forceinline__ void convert_item(Frame& F, int i0, LAS unsigned char* cvbuf) {
;     ...
;             for (int q = 0; q < 8; ++q) { v4u o; o.x = pk4f8(x[16 * q + 0] * F8_SW, x[16 * q + 1] * F8_SW, x[16 * q + 2] * F8_SW, x[16 * q + 3] * F8_SW); o.y = pk4f8(x[16 * q + 4] * F8_SW, x[16 * q + 5] * F8_SW, x[16 * q + 6] * F8_SW, x[16 * q + 7] * F8_SW);
;                 o.z = pk4f8(x[16 * q + 8] * F8_SW, x[16 * q + 9] * F8_SW, x[16 * q + 10] * F8_SW, x[16 * q + 11] * F8_SW); o.w = pk4f8(x[16 * q + 12] * F8_SW, x[16 * q + 13] * F8_SW, x[16 * q + 14] * F8_SW, x[16 * q + 15] * F8_SW);
;                 *(LAS v4u*)(bw + 16 * q) = o; }
;             unsigned char* d0 = c.dst - (size_t)lane * 2048 + (size_t)(lane >> 3) * 2048 + (lane & 7) * 16; const LAS unsigned char* br = cvbuf + (lane >> 3) * 144 + (lane & 7) * 16;
; #pragma unroll
;             for (int i = 0; i < 8; ++i) { const v4u v = *(const LAS v4u*)(br + i * 8 * 144); *(v4u*)(d0 + (size_t)i * 8 * 2048) = v; } }
	v_mul_f32_e32 v148, 0x43800000, v94
	v_mov_b32_e32 v146, v3
	v_cvt_pk_fp8_f32 v146, v147, v148
	s_waitcnt vmcnt(43)
	v_mul_f32_e32 v148, 0x43800000, v98
	s_waitcnt vmcnt(42)
	v_mul_f32_e32 v151, 0x43800000, v100
	v_mov_b32_e32 v147, v3
	v_cvt_pk_fp8_f32 v147, v148, v151
	v_mul_f32_e32 v149, 0x43800000, v95
	v_mul_f32_e32 v150, 0x43800000, v97
	v_cvt_pk_fp8_f32 v146, v149, v150 op_sel:[0,0,1]
	s_waitcnt vmcnt(41)
	v_mul_f32_e32 v148, 0x43800000, v101
	s_waitcnt vmcnt(40)
	v_mul_f32_e32 v149, 0x43800000, v104
	v_cvt_pk_fp8_f32 v147, v148, v149 op_sel:[0,0,1]
	s_waitcnt vmcnt(39)
	v_mul_f32_e32 v149, 0x43800000, v99
	s_waitcnt vmcnt(38)
	v_mul_f32_e32 v150, 0x43800000, v102
	v_mov_b32_e32 v148, v3
	v_cvt_pk_fp8_f32 v148, v149, v150
	s_waitcnt vmcnt(35)
	v_mul_f32_e32 v150, 0x43800000, v106
	s_waitcnt vmcnt(34)
	v_mul_f32_e32 v153, 0x43800000, v108
	v_mov_b32_e32 v149, v3
	v_cvt_pk_fp8_f32 v149, v150, v153
	v_mul_f32_e32 v151, 0x43800000, v103
	v_mul_f32_e32 v152, 0x43800000, v105
	v_cvt_pk_fp8_f32 v148, v151, v152 op_sel:[0,0,1]
	s_waitcnt vmcnt(33)
	v_mul_f32_e32 v150, 0x43800000, v109
	s_waitcnt vmcnt(32)
	v_mul_f32_e32 v151, 0x43800000, v112
	v_cvt_pk_fp8_f32 v149, v150, v151 op_sel:[0,0,1]
	s_waitcnt vmcnt(31)
	v_mul_f32_e32 v151, 0x43800000, v107
	s_waitcnt vmcnt(30)
	v_mul_f32_e32 v152, 0x43800000, v110
	v_mov_b32_e32 v150, v3
	v_cvt_pk_fp8_f32 v150, v151, v152
	s_waitcnt vmcnt(27)
	v_mul_f32_e32 v152, 0x43800000, v114
	s_waitcnt vmcnt(26)
	v_mul_f32_e32 v155, 0x43800000, v116
	v_mov_b32_e32 v151, v3
	v_cvt_pk_fp8_f32 v151, v152, v155
	v_mul_f32_e32 v153, 0x43800000, v111
	v_mul_f32_e32 v154, 0x43800000, v113
	v_cvt_pk_fp8_f32 v150, v153, v154 op_sel:[0,0,1]
	s_waitcnt vmcnt(25)
	v_mul_f32_e32 v152, 0x43800000, v117
	s_waitcnt vmcnt(24)
	v_mul_f32_e32 v153, 0x43800000, v120
	v_cvt_pk_fp8_f32 v151, v152, v153 op_sel:[0,0,1]
	s_waitcnt vmcnt(23)
	v_mul_f32_e32 v153, 0x43800000, v115
	s_waitcnt vmcnt(22)
	v_mul_f32_e32 v154, 0x43800000, v118
	v_mov_b32_e32 v152, v3
	v_cvt_pk_fp8_f32 v152, v153, v154
	s_waitcnt vmcnt(19)
	v_mul_f32_e32 v154, 0x43800000, v122
	s_waitcnt vmcnt(18)
	v_mul_f32_e32 v157, 0x43800000, v124
	v_mov_b32_e32 v153, v3
	v_cvt_pk_fp8_f32 v153, v154, v157
	v_mul_f32_e32 v155, 0x43800000, v119
	v_mul_f32_e32 v156, 0x43800000, v121
	v_cvt_pk_fp8_f32 v152, v155, v156 op_sel:[0,0,1]
	s_waitcnt vmcnt(17)
	v_mul_f32_e32 v154, 0x43800000, v125
	s_waitcnt vmcnt(16)
	v_mul_f32_e32 v155, 0x43800000, v128
	v_cvt_pk_fp8_f32 v153, v154, v155 op_sel:[0,0,1]
	s_waitcnt vmcnt(15)
	v_mul_f32_e32 v155, 0x43800000, v123
	s_waitcnt vmcnt(14)
	v_mul_f32_e32 v156, 0x43800000, v126
	v_mov_b32_e32 v154, v3
	v_cvt_pk_fp8_f32 v154, v155, v156
	s_waitcnt vmcnt(11)
	v_mul_f32_e32 v156, 0x43800000, v130
	s_waitcnt vmcnt(10)
	v_mul_f32_e32 v159, 0x43800000, v132
	v_mov_b32_e32 v155, v3
	v_cvt_pk_fp8_f32 v155, v156, v159
	v_mul_f32_e32 v157, 0x43800000, v127
	v_mul_f32_e32 v158, 0x43800000, v129
	v_cvt_pk_fp8_f32 v154, v157, v158 op_sel:[0,0,1]
	s_waitcnt vmcnt(9)
	v_mul_f32_e32 v156, 0x43800000, v133
	s_waitcnt vmcnt(8)
	v_mul_f32_e32 v157, 0x43800000, v136
	v_cvt_pk_fp8_f32 v155, v156, v157 op_sel:[0,0,1]
	s_waitcnt vmcnt(7)
	v_mul_f32_e32 v157, 0x43800000, v131
	s_waitcnt vmcnt(6)
	v_mul_f32_e32 v158, 0x43800000, v134
	v_mov_b32_e32 v156, v3
	v_cvt_pk_fp8_f32 v156, v157, v158
	s_waitcnt vmcnt(3)
	v_mul_f32_e32 v158, 0x43800000, v138
	s_waitcnt vmcnt(2)
	v_mul_f32_e32 v161, 0x43800000, v139
	v_mov_b32_e32 v157, v3
	v_cvt_pk_fp8_f32 v157, v158, v161
	v_mul_f32_e32 v159, 0x43800000, v135
	v_mul_f32_e32 v160, 0x43800000, v137
	v_cvt_pk_fp8_f32 v156, v159, v160 op_sel:[0,0,1]
	s_waitcnt vmcnt(1)
	v_mul_f32_e32 v158, 0x43800000, v140
	s_waitcnt vmcnt(0)
	v_mul_f32_e32 v159, 0x43800000, v141
	v_cvt_pk_fp8_f32 v157, v158, v159 op_sel:[0,0,1]
	ds_write_b128 v14, v[142:145] offset:8256
	ds_write_b128 v14, v[146:149] offset:8272
	ds_write_b128 v14, v[150:153] offset:8288
	ds_write_b128 v14, v[154:157] offset:8304
	ds_read_b128 v[142:145], v15 offset:8192
	v_lshl_add_u64 v[146:147], v[10:11], 0, v[4:5]
	v_lshl_add_u64 v[146:147], v[146:147], 0, v[6:7]
	v_lshl_add_u64 v[150:151], v[146:147], 0, v[8:9]
	ds_read_b128 v[146:149], v15 offset:9344
	s_waitcnt lgkmcnt(1)
	global_store_dwordx4 v[150:151], v[142:145], off nt
	s_mov_b64 s[14:15], 0
	s_nop 0
	v_add_co_u32_e32 v142, vcc, s24, v150
	s_nop 1
	v_addc_co_u32_e32 v143, vcc, 0, v151, vcc
	s_waitcnt lgkmcnt(0)
	global_store_dwordx4 v[142:143], v[146:149], off nt
	ds_read_b128 v[142:145], v15 offset:10496
	ds_read_b128 v[146:149], v15 offset:11648
	v_add_co_u32_e32 v152, vcc, s25, v150
	s_nop 1
	v_addc_co_u32_e32 v153, vcc, 0, v151, vcc
	s_waitcnt lgkmcnt(1)
	global_store_dwordx4 v[152:153], v[142:145], off nt
	s_nop 1
	v_add_co_u32_e32 v142, vcc, s26, v150
	s_nop 1
	v_addc_co_u32_e32 v143, vcc, 0, v151, vcc
	s_waitcnt lgkmcnt(0)
	global_store_dwordx4 v[142:143], v[146:149], off nt
	ds_read_b128 v[142:145], v15 offset:12800
	ds_read_b128 v[146:149], v15 offset:13952
	v_add_co_u32_e32 v152, vcc, s27, v150
	s_nop 1
	v_addc_co_u32_e32 v153, vcc, 0, v151, vcc
	s_waitcnt lgkmcnt(1)
	global_store_dwordx4 v[152:153], v[142:145], off nt
	s_nop 1
	v_add_co_u32_e32 v142, vcc, 0x14000, v150
	s_nop 1
	v_addc_co_u32_e32 v143, vcc, 0, v151, vcc
	s_waitcnt lgkmcnt(0)
	global_store_dwordx4 v[142:143], v[146:149], off nt
	ds_read_b128 v[142:145], v15 offset:15104
	ds_read_b128 v[146:149], v15 offset:16256
	v_add_co_u32_e32 v152, vcc, 0x18000, v150
	s_nop 1
	v_addc_co_u32_e32 v153, vcc, 0, v151, vcc
	s_waitcnt lgkmcnt(1)
	global_store_dwordx4 v[152:153], v[142:145], off nt
	s_nop 1
	v_add_co_u32_e32 v142, vcc, 0x1c000, v150
	s_nop 1
	v_addc_co_u32_e32 v143, vcc, 0, v151, vcc
	s_waitcnt lgkmcnt(0)
	global_store_dwordx4 v[142:143], v[146:149], off nt
; __device__ __forceinline__ unsigned pk2(float lo, float hi) { const f32x2 v = {lo, hi}; const bf16x2_t b = __builtin_convertvector(v, bf16x2_t); return __builtin_bit_cast(unsigned, b); }
; __device__ __forceinline__ void convert_item(Frame& F, int i0, LAS unsigned char* cvbuf) {
;     ...
;         else {
; #pragma unroll
;             for (int q = 0; q < 16; ++q) { v4u o; o.x = pk2(x[8 * q + 0], x[8 * q + 1]); o.y = pk2(x[8 * q + 2], x[8 * q + 3]); o.z = pk2(x[8 * q + 4], x[8 * q + 5]); o.w = pk2(x[8 * q + 6], x[8 * q + 7]);
;                 *(v4u*)(c.dst + 16 * q) = o; } } }
.LBB0_1094:
	s_andn2_b64 vcc, exec, s[14:15]
	s_cbranch_vccnz .LBB0_1071
	v_cvt_pk_bf16_f32 v16, v16, v13
	v_cvt_pk_bf16_f32 v17, v17, v18
	v_cvt_pk_bf16_f32 v18, v19, v20
	v_cvt_pk_bf16_f32 v19, v21, v24
	global_store_dwordx4 v[10:11], v[16:19], off nt
	s_nop 1
	v_cvt_pk_bf16_f32 v16, v12, v22
	v_cvt_pk_bf16_f32 v17, v23, v25
	v_cvt_pk_bf16_f32 v18, v26, v28
	v_cvt_pk_bf16_f32 v19, v29, v32
	global_store_dwordx4 v[10:11], v[16:19], off offset:16 nt
	s_nop 1
	v_cvt_pk_bf16_f32 v16, v27, v30
	v_cvt_pk_bf16_f32 v17, v31, v33
	v_cvt_pk_bf16_f32 v18, v34, v36
	v_cvt_pk_bf16_f32 v19, v37, v40
	global_store_dwordx4 v[10:11], v[16:19], off offset:32 nt
	s_nop 1
	v_cvt_pk_bf16_f32 v16, v35, v38
	v_cvt_pk_bf16_f32 v17, v39, v41
	v_cvt_pk_bf16_f32 v18, v42, v44
	v_cvt_pk_bf16_f32 v19, v45, v48
	global_store_dwordx4 v[10:11], v[16:19], off offset:48 nt
	s_nop 1
	v_cvt_pk_bf16_f32 v16, v43, v46
	v_cvt_pk_bf16_f32 v17, v47, v49
	v_cvt_pk_bf16_f32 v18, v50, v52
	v_cvt_pk_bf16_f32 v19, v53, v56
	global_store_dwordx4 v[10:11], v[16:19], off offset:64 nt
	s_nop 1
	v_cvt_pk_bf16_f32 v16, v51, v54
	v_cvt_pk_bf16_f32 v17, v55, v57
	v_cvt_pk_bf16_f32 v18, v58, v60
	v_cvt_pk_bf16_f32 v19, v61, v64
	global_store_dwordx4 v[10:11], v[16:19], off offset:80 nt
	s_nop 1
	v_cvt_pk_bf16_f32 v16, v59, v62
	v_cvt_pk_bf16_f32 v17, v63, v65
	v_cvt_pk_bf16_f32 v18, v66, v68
	v_cvt_pk_bf16_f32 v19, v69, v72
	global_store_dwordx4 v[10:11], v[16:19], off offset:96 nt
	s_nop 1
	v_cvt_pk_bf16_f32 v16, v67, v70
	v_cvt_pk_bf16_f32 v17, v71, v73
	s_waitcnt vmcnt(62)
	v_cvt_pk_bf16_f32 v18, v74, v76
	v_cvt_pk_bf16_f32 v19, v77, v80
	global_store_dwordx4 v[10:11], v[16:19], off offset:112 nt
	s_nop 1
	v_cvt_pk_bf16_f32 v16, v75, v78
	v_cvt_pk_bf16_f32 v17, v79, v81
	v_cvt_pk_bf16_f32 v18, v82, v84
	v_cvt_pk_bf16_f32 v19, v85, v88
	global_store_dwordx4 v[10:11], v[16:19], off offset:128 nt
	s_waitcnt vmcnt(62)
	s_nop 0
	v_cvt_pk_bf16_f32 v16, v83, v86
	s_waitcnt vmcnt(61)
	v_cvt_pk_bf16_f32 v17, v87, v89
	s_waitcnt vmcnt(59)
	v_cvt_pk_bf16_f32 v18, v90, v92
	s_waitcnt vmcnt(57)
	v_cvt_pk_bf16_f32 v19, v93, v96
	global_store_dwordx4 v[10:11], v[16:19], off offset:144 nt
	s_waitcnt vmcnt(56)
	s_nop 0
	v_cvt_pk_bf16_f32 v16, v91, v94
	s_waitcnt vmcnt(54)
	v_cvt_pk_bf16_f32 v17, v95, v97
	s_waitcnt vmcnt(52)
	v_cvt_pk_bf16_f32 v18, v98, v100
	s_waitcnt vmcnt(50)
	v_cvt_pk_bf16_f32 v19, v101, v104
	global_store_dwordx4 v[10:11], v[16:19], off offset:160 nt
	s_waitcnt vmcnt(49)
	s_nop 0
	v_cvt_pk_bf16_f32 v16, v99, v102
	s_waitcnt vmcnt(47)
	v_cvt_pk_bf16_f32 v17, v103, v105
	s_waitcnt vmcnt(45)
	v_cvt_pk_bf16_f32 v18, v106, v108
	s_waitcnt vmcnt(43)
	v_cvt_pk_bf16_f32 v19, v109, v112
	global_store_dwordx4 v[10:11], v[16:19], off offset:176 nt
	s_waitcnt vmcnt(42)
	s_nop 0
	v_cvt_pk_bf16_f32 v16, v107, v110
	s_waitcnt vmcnt(40)
	v_cvt_pk_bf16_f32 v17, v111, v113
	s_waitcnt vmcnt(38)
	v_cvt_pk_bf16_f32 v18, v114, v116
	s_waitcnt vmcnt(36)
	v_cvt_pk_bf16_f32 v19, v117, v120
	global_store_dwordx4 v[10:11], v[16:19], off offset:192 nt
	s_waitcnt vmcnt(35)
	s_nop 0
	v_cvt_pk_bf16_f32 v16, v115, v118
	s_waitcnt vmcnt(33)
	v_cvt_pk_bf16_f32 v17, v119, v121
	s_waitcnt vmcnt(31)
	v_cvt_pk_bf16_f32 v18, v122, v124
	s_waitcnt vmcnt(29)
	v_cvt_pk_bf16_f32 v19, v125, v128
	global_store_dwordx4 v[10:11], v[16:19], off offset:208 nt
	s_waitcnt vmcnt(28)
	s_nop 0
	v_cvt_pk_bf16_f32 v16, v123, v126
	s_waitcnt vmcnt(26)
	v_cvt_pk_bf16_f32 v17, v127, v129
	s_waitcnt vmcnt(24)
	v_cvt_pk_bf16_f32 v18, v130, v132
	s_waitcnt vmcnt(22)
	v_cvt_pk_bf16_f32 v19, v133, v136
	global_store_dwordx4 v[10:11], v[16:19], off offset:224 nt
	s_waitcnt vmcnt(21)
	s_nop 0
	v_cvt_pk_bf16_f32 v16, v131, v134
	s_waitcnt vmcnt(19)
	v_cvt_pk_bf16_f32 v17, v135, v137
	s_waitcnt vmcnt(17)
	v_cvt_pk_bf16_f32 v18, v138, v139
	s_waitcnt vmcnt(15)
	v_cvt_pk_bf16_f32 v19, v140, v141
	global_store_dwordx4 v[10:11], v[16:19], off offset:240 nt
	s_branch .LBB0_1071
